# k_csr: CSR segment write-out issues all LDS reads before the (write-through) stores instead of a read-wait-store loop
# baseline (speedup 1.0000x reference)
.LBB1_226:
	s_mov_b64 s[6:7], exec
	ds_read_b128 v[6:9], v2
	v_add_u32_e32 v10, 0x100, v0
	v_add_u32_e32 v11, 0x200, v0
	v_add_u32_e32 v12, 0x300, v0
	v_cmp_gt_i32_e64 s[8:9], s4, v10
	v_cmp_gt_i32_e64 s[10:11], s4, v11
	v_cmp_gt_i32_e64 s[12:13], s4, v12
	v_lshl_add_u64 v[26:27], v[4:5], 0, s[2:3]
	v_lshl_add_u64 v[28:29], v[26:27], 0, s[2:3]
	v_lshl_add_u64 v[30:31], v[28:29], 0, s[2:3]
	s_mov_b64 exec, s[8:9]
	ds_read_b128 v[14:17], v2 offset:4096
	s_mov_b64 exec, s[10:11]
	ds_read_b128 v[18:21], v2 offset:8192
	s_mov_b64 exec, s[12:13]
	ds_read_b128 v[22:25], v2 offset:12288
	s_mov_b64 exec, s[6:7]
	s_waitcnt lgkmcnt(0)
	global_store_dwordx4 v[4:5], v[6:9], off sc1
	s_mov_b64 exec, s[8:9]
	global_store_dwordx4 v[26:27], v[14:17], off sc1
	s_mov_b64 exec, s[10:11]
	global_store_dwordx4 v[28:29], v[18:21], off sc1
	s_mov_b64 exec, s[12:13]
	global_store_dwordx4 v[30:31], v[22:25], off sc1
